# attention loop: mask-word load queued behind the step's two LDS-DMA pieces, closing waits count three, counted wait before the word's first use: the mask word gets two steps to land instead of one
# speedup vs baseline: 1.0107x; 1.0107x over previous
; #define WAIT_BAR(N) asm volatile("s_waitcnt vmcnt(" #N ") lgkmcnt(0)\n\ts_barrier":::"memory")
;   #define RESC() do{ if(resc){ asm volatile("s_waitcnt lgkmcnt(0)":::"memory"); \
;       _Pragma("unroll") for(int d_=0;d_<2;++d_) _Pragma("unroll") for(int r=0;r<16;++r)o[d_][r]*=wsf[crow(r,hi)]; } }while(0)
;   #define ROT() do{sl_prev=sl_cur;sl_cur=sl_next;sl_next=(sl_next==(NSLOT-1)*SLOTB)?0:sl_next+SLOTB;}while(0)
; template<int THRL> __device__ __forceinline__ void attn_unit(int b,int h,int qb,const bf16*Q,const bf16*__restrict__ K,const bf16*__restrict__ V,bf16*O,const unsigned*MASK,char*shm){
;     ...
;   int t=1;
;   for(;t+5<NT;t+=2){
;     STEP(pB0,pB1,pA0,pA1,t,true,true,true,wB,wA);     WAIT_BAR(2); RESC(); ROT();
.LBB0_1273:
	s_movk_i32 s42, 0xff00
	s_mov_b32 s43, -1
	v_lshl_add_u64 v[86:87], v[192:193], 0, s[42:43]
	v_lshl_add_u64 v[222:223], v[188:189], 0, s[86:87]
	s_add_i32 s63, s47, s58
	s_mov_b32 m0, s63
	s_nop 0
	global_load_lds_dwordx4 v[222:223], off
	v_lshl_add_u64 v[222:223], v[190:191], 0, s[86:87]
	s_add_i32 s63, s48, s59
	s_mov_b32 m0, s63
	s_nop 0
	global_load_lds_dwordx4 v[222:223], off
	global_load_dword v2, v[86:87], off
	v_add_u32_e32 v255, s4, v220
	ds_read_b64_tr_b16 v[182:183], v255 offset:24576
	ds_read_b64_tr_b16 v[184:185], v255 offset:25088
	s_waitcnt lgkmcnt(9)
	v_mfma_f32_32x32x16_bf16 v[102:117], v[178:181], v[138:141], v[36:51]
	v_cvt_pk_bf16_f32 v146, v68, v69
	v_cvt_pk_bf16_f32 v147, v70, v71
	ds_read_b64_tr_b16 v[178:179], v255 offset:28672
	ds_read_b64_tr_b16 v[180:181], v255 offset:29184
	s_waitcnt lgkmcnt(10)
	v_mfma_f32_32x32x16_bf16 v[86:101], v[170:173], v[138:141], v[36:51]
	v_cvt_pk_bf16_f32 v148, v72, v73
	v_cvt_pk_bf16_f32 v149, v74, v75
	ds_read_b64_tr_b16 v[170:171], v255 offset:25600
	ds_read_b64_tr_b16 v[172:173], v255 offset:26112
	s_waitcnt lgkmcnt(11)
	v_mfma_f32_32x32x16_bf16 v[102:117], v[174:177], v[134:137], v[102:117]
	v_cvt_pk_bf16_f32 v142, v76, v77
	v_cvt_pk_bf16_f32 v143, v78, v79
	ds_read_b64_tr_b16 v[76:77], v255 offset:29696
	ds_read_b64_tr_b16 v[78:79], v255 offset:30208
	s_waitcnt lgkmcnt(12)
	v_mfma_f32_32x32x16_bf16 v[86:101], v[162:165], v[134:137], v[86:101]
	v_cvt_pk_bf16_f32 v144, v80, v81
	v_cvt_pk_bf16_f32 v145, v82, v83
	ds_read_b64_tr_b16 v[72:73], v255 offset:26624
	ds_read_b64_tr_b16 v[74:75], v255 offset:27136
	s_waitcnt lgkmcnt(13)
	v_mfma_f32_32x32x16_bf16 v[102:117], v[166:169], v[126:129], v[102:117]
	v_cvt_pk_bf16_f32 v130, v52, v53
	v_cvt_pk_bf16_f32 v131, v54, v55
	ds_read_b64_tr_b16 v[68:69], v255 offset:30720
	ds_read_b64_tr_b16 v[70:71], v255 offset:31232
	s_waitcnt lgkmcnt(14)
	v_mfma_f32_32x32x16_bf16 v[86:101], v[154:157], v[126:129], v[86:101]
	v_cvt_pk_bf16_f32 v132, v56, v57
	v_cvt_pk_bf16_f32 v133, v58, v59
	ds_read_b64_tr_b16 v[56:57], v255 offset:27648
	ds_read_b64_tr_b16 v[58:59], v255 offset:28160
	s_waitcnt lgkmcnt(14)
	v_mfma_f32_32x32x16_bf16 v[102:117], v[158:161], v[122:125], v[102:117]
	v_cvt_pk_bf16_f32 v118, v60, v61
	v_cvt_pk_bf16_f32 v119, v62, v63
	ds_read_b64_tr_b16 v[52:53], v255 offset:31744
	ds_read_b64_tr_b16 v[54:55], v255 offset:32256
	v_mfma_f32_32x32x16_bf16 v[86:101], v[150:153], v[122:125], v[86:101]
	v_cvt_pk_bf16_f32 v120, v64, v65
	v_cvt_pk_bf16_f32 v121, v66, v67
	ds_read_b128 v[80:83], v225 offset:51200
	v_max_f32_e32 v60, v103, v103
	v_max_f32_e32 v61, v102, v102
	v_max_f32_e32 v60, v61, v60
	v_max3_f32 v61, v104, v105, v87
	v_max3_f32 v60, v60, v86, v88
	v_max3_f32 v60, v60, v89, v106
	v_max3_f32 v61, v61, v108, v109
	v_max3_f32 v60, v60, v107, v90
	v_max3_f32 v61, v61, v92, v93
	v_max3_f32 v60, v60, v91, v110
	v_max3_f32 v61, v61, v112, v113
	v_max3_f32 v60, v60, v111, v94
	v_max3_f32 v61, v61, v96, v97
	v_max3_f32 v60, v60, v95, v114
	v_max3_f32 v61, v61, v116, v117
	v_max3_f32 v60, v60, v115, v98
	v_max3_f32 v61, v61, v100, v101
	v_max3_f32 v60, v60, v99, v61
	v_mov_b32_e32 v61, v60
	s_nop 1
	v_permlane32_swap_b32_e32 v60, v61
	v_max_f32_e32 v61, v61, v61
	v_max_f32_e32 v60, v60, v60
	v_max_f32_e32 v60, v60, v61
	v_cmp_lt_f32_e32 vcc, s14, v60
	s_cmp_lg_u64 vcc, 0
	s_cselect_b64 s[42:43], -1, 0
	s_cbranch_vccnz .LBB0_1281
.LBB0_1274:
	s_waitcnt lgkmcnt(0)
	v_and_b32_e32 v146, v146, v80
	v_and_b32_e32 v147, v147, v81
	v_and_b32_e32 v148, v148, v82
	v_and_b32_e32 v149, v149, v83
	ds_read_b128 v[80:83], v226 offset:51200
	s_waitcnt lgkmcnt(14)
	v_mfma_f32_32x32x16_bf16 v[20:35], v[146:149], v[182:185], v[20:35]
	v_exp_f32_e32 v102, v102
	v_exp_f32_e32 v103, v103
	v_exp_f32_e32 v104, v104
	v_exp_f32_e32 v105, v105
	s_waitcnt lgkmcnt(12)
	v_mfma_f32_32x32x16_bf16 v[4:19], v[146:149], v[178:181], v[4:19]
	v_mfma_f32_32x32x16_bf16 v[228:243], v[146:149], v[204:207], v[228:243]
	v_exp_f32_e32 v106, v106
	v_exp_f32_e32 v107, v107
	v_exp_f32_e32 v108, v108
	v_exp_f32_e32 v109, v109
	s_waitcnt lgkmcnt(0)
	v_and_b32_e32 v142, v142, v80
	v_and_b32_e32 v143, v143, v81
	v_and_b32_e32 v144, v144, v82
	v_and_b32_e32 v145, v145, v83
	ds_read_b128 v[80:83], v248 offset:51200
	v_add_u32_e32 v64, s48, v221
	ds_read_b128 v[60:63], v64
	ds_read_b128 v[150:153], v64 offset:512
	s_waitcnt lgkmcnt(12)
	v_mfma_f32_32x32x16_bf16 v[20:35], v[142:145], v[170:173], v[20:35]
	v_exp_f32_e32 v110, v110
	v_exp_f32_e32 v111, v111
	v_exp_f32_e32 v112, v112
	v_exp_f32_e32 v113, v113
	ds_read_b128 v[174:177], v64 offset:2048
	ds_read_b128 v[162:165], v64 offset:2560
	s_waitcnt lgkmcnt(12)
	v_mfma_f32_32x32x16_bf16 v[4:19], v[142:145], v[76:79], v[4:19]
	v_mfma_f32_32x32x16_bf16 v[228:243], v[142:145], v[204:207], v[228:243]
	v_exp_f32_e32 v114, v114
	v_exp_f32_e32 v115, v115
	v_exp_f32_e32 v116, v116
	v_exp_f32_e32 v117, v117
	s_waitcnt lgkmcnt(4)
	v_and_b32_e32 v130, v130, v80
	v_and_b32_e32 v131, v131, v81
	v_and_b32_e32 v132, v132, v82
	v_and_b32_e32 v133, v133, v83
	ds_read_b128 v[80:83], v249 offset:51200
	ds_read_b128 v[170:173], v64 offset:4096
	ds_read_b128 v[158:161], v64 offset:4608
	s_waitcnt lgkmcnt(12)
	v_mfma_f32_32x32x16_bf16 v[20:35], v[130:133], v[72:75], v[20:35]
	v_exp_f32_e32 v86, v86
	v_exp_f32_e32 v87, v87
	v_exp_f32_e32 v88, v88
	v_exp_f32_e32 v89, v89
	ds_read_b128 v[166:169], v64 offset:6144
	ds_read_b128 v[154:157], v64 offset:6656
	s_waitcnt lgkmcnt(12)
	v_mfma_f32_32x32x16_bf16 v[4:19], v[130:133], v[68:71], v[4:19]
	v_mfma_f32_32x32x16_bf16 v[228:243], v[130:133], v[204:207], v[228:243]
	v_exp_f32_e32 v90, v90
	v_exp_f32_e32 v91, v91
	v_exp_f32_e32 v92, v92
	v_exp_f32_e32 v93, v93
	s_waitcnt lgkmcnt(4)
	v_and_b32_e32 v118, v118, v80
	v_and_b32_e32 v119, v119, v81
	v_and_b32_e32 v120, v120, v82
	v_and_b32_e32 v121, v121, v83
	s_nop 0
	s_waitcnt lgkmcnt(10)
	v_mfma_f32_32x32x16_bf16 v[20:35], v[118:121], v[56:59], v[20:35]
	v_exp_f32_e32 v94, v94
	v_exp_f32_e32 v95, v95
	v_exp_f32_e32 v96, v96
	v_exp_f32_e32 v97, v97
	s_waitcnt lgkmcnt(8)
	v_mfma_f32_32x32x16_bf16 v[4:19], v[118:121], v[52:55], v[4:19]
	v_mfma_f32_32x32x16_bf16 v[228:243], v[118:121], v[204:207], v[228:243]
	v_exp_f32_e32 v98, v98
	v_exp_f32_e32 v99, v99
	v_exp_f32_e32 v100, v100
	v_exp_f32_e32 v101, v101
	s_waitcnt vmcnt(3)
	v_lshlrev_b32_sdwa v225, s32, v218 dst_sel:DWORD dst_unused:UNUSED_PAD src0_sel:DWORD src1_sel:BYTE_0
	v_lshlrev_b32_sdwa v226, s32, v218 dst_sel:DWORD dst_unused:UNUSED_PAD src0_sel:DWORD src1_sel:BYTE_1
	v_lshlrev_b32_sdwa v248, s32, v218 dst_sel:DWORD dst_unused:UNUSED_PAD src0_sel:DWORD src1_sel:BYTE_2
	v_lshlrev_b32_sdwa v249, s32, v218 dst_sel:DWORD dst_unused:UNUSED_PAD src0_sel:DWORD src1_sel:BYTE_3
	s_waitcnt vmcnt(3) lgkmcnt(0)
	s_barrier
	s_andn2_b64 vcc, exec, s[42:43]
	s_cbranch_vccnz .LBB0_1276
	s_waitcnt lgkmcnt(0)
	ds_read_b128 v[52:55], v85 offset:49248
	ds_read_b128 v[56:59], v85 offset:49216
	ds_read_b128 v[64:67], v85 offset:49184
	ds_read_b128 v[68:71], v85 offset:49152
	s_waitcnt lgkmcnt(3)
	v_pk_mul_f32 v[32:33], v[32:33], v[52:53]
	s_waitcnt lgkmcnt(2)
	v_pk_mul_f32 v[28:29], v[28:29], v[56:57]
	s_waitcnt lgkmcnt(1)
	v_pk_mul_f32 v[24:25], v[24:25], v[64:65]
	v_pk_mul_f32 v[34:35], v[34:35], v[54:55]
	v_pk_mul_f32 v[30:31], v[30:31], v[58:59]
	v_pk_mul_f32 v[26:27], v[26:27], v[66:67]
	s_waitcnt lgkmcnt(0)
	v_pk_mul_f32 v[22:23], v[22:23], v[70:71]
	v_pk_mul_f32 v[20:21], v[20:21], v[68:69]
	v_pk_mul_f32 v[16:17], v[16:17], v[52:53]
	v_pk_mul_f32 v[12:13], v[12:13], v[56:57]
	v_pk_mul_f32 v[8:9], v[8:9], v[64:65]
	v_pk_mul_f32 v[18:19], v[18:19], v[54:55]
	v_pk_mul_f32 v[14:15], v[14:15], v[58:59]
	v_pk_mul_f32 v[10:11], v[10:11], v[66:67]
	v_pk_mul_f32 v[6:7], v[6:7], v[70:71]
	v_pk_mul_f32 v[4:5], v[4:5], v[68:69]
	v_pk_mul_f32 v[240:241], v[240:241], v[52:53]
	v_pk_mul_f32 v[236:237], v[236:237], v[56:57]
	v_pk_mul_f32 v[232:233], v[232:233], v[64:65]
	v_pk_mul_f32 v[242:243], v[242:243], v[54:55]
	v_pk_mul_f32 v[238:239], v[238:239], v[58:59]
	v_pk_mul_f32 v[234:235], v[234:235], v[66:67]
	v_pk_mul_f32 v[230:231], v[230:231], v[70:71]
	v_pk_mul_f32 v[228:229], v[228:229], v[68:69]
.LBB0_1276:
	s_add_i32 s4, s48, 0x2000
	s_cmpk_lg_i32 s48, 0x4000
	s_cselect_b32 s60, s4, 0
	s_add_i32 s63, s48, s58
	s_mov_b32 m0, s63
	s_nop 0
	global_load_lds_dwordx4 v[188:189], off
	s_add_i32 s63, s60, s59
	s_mov_b32 m0, s63
	s_nop 0
	global_load_lds_dwordx4 v[190:191], off
	global_load_dword v218, v[192:193], off
	v_add_u32_e32 v255, s47, v220
	ds_read_b64_tr_b16 v[182:183], v255 offset:24576
	ds_read_b64_tr_b16 v[184:185], v255 offset:25088
	s_waitcnt lgkmcnt(9)
	v_mfma_f32_32x32x16_bf16 v[68:83], v[60:63], v[138:141], v[36:51]
	v_cvt_pk_bf16_f32 v146, v102, v103
	v_cvt_pk_bf16_f32 v147, v104, v105
	ds_read_b64_tr_b16 v[178:179], v255 offset:28672
	ds_read_b64_tr_b16 v[180:181], v255 offset:29184
	s_waitcnt lgkmcnt(10)
	v_mfma_f32_32x32x16_bf16 v[52:67], v[150:153], v[138:141], v[36:51]
	v_cvt_pk_bf16_f32 v148, v106, v107
	v_cvt_pk_bf16_f32 v149, v108, v109
	ds_read_b64_tr_b16 v[150:151], v255 offset:25600
	ds_read_b64_tr_b16 v[152:153], v255 offset:26112
	s_waitcnt lgkmcnt(11)
	v_mfma_f32_32x32x16_bf16 v[68:83], v[174:177], v[134:137], v[68:83]
	v_cvt_pk_bf16_f32 v142, v110, v111
	v_cvt_pk_bf16_f32 v143, v112, v113
	ds_read_b64_tr_b16 v[110:111], v255 offset:29696
	ds_read_b64_tr_b16 v[112:113], v255 offset:30208
	s_waitcnt lgkmcnt(12)
	v_mfma_f32_32x32x16_bf16 v[52:67], v[162:165], v[134:137], v[52:67]
	v_cvt_pk_bf16_f32 v144, v114, v115
	v_cvt_pk_bf16_f32 v145, v116, v117
	ds_read_b64_tr_b16 v[106:107], v255 offset:26624
	ds_read_b64_tr_b16 v[108:109], v255 offset:27136
	s_waitcnt lgkmcnt(13)
	v_mfma_f32_32x32x16_bf16 v[68:83], v[170:173], v[126:129], v[68:83]
	v_cvt_pk_bf16_f32 v130, v86, v87
	v_cvt_pk_bf16_f32 v131, v88, v89
	ds_read_b64_tr_b16 v[102:103], v255 offset:30720
	ds_read_b64_tr_b16 v[104:105], v255 offset:31232
	s_waitcnt lgkmcnt(14)
	v_mfma_f32_32x32x16_bf16 v[52:67], v[158:161], v[126:129], v[52:67]
	v_cvt_pk_bf16_f32 v132, v90, v91
	v_cvt_pk_bf16_f32 v133, v92, v93
	ds_read_b64_tr_b16 v[90:91], v255 offset:27648
	ds_read_b64_tr_b16 v[92:93], v255 offset:28160
	s_waitcnt lgkmcnt(14)
	v_mfma_f32_32x32x16_bf16 v[68:83], v[166:169], v[122:125], v[68:83]
	v_cvt_pk_bf16_f32 v118, v94, v95
	v_cvt_pk_bf16_f32 v119, v96, v97
	ds_read_b64_tr_b16 v[86:87], v255 offset:31744
	ds_read_b64_tr_b16 v[88:89], v255 offset:32256
	v_mfma_f32_32x32x16_bf16 v[52:67], v[154:157], v[122:125], v[52:67]
	v_cvt_pk_bf16_f32 v120, v98, v99
	v_cvt_pk_bf16_f32 v121, v100, v101
	ds_read_b128 v[114:117], v225 offset:51200
	v_max_f32_e32 v95, v69, v69
	v_max_f32_e32 v96, v68, v68
	v_max_f32_e32 v95, v96, v95
	s_nop 3
	v_max3_f32 v96, v70, v71, v53
	v_max3_f32 v95, v95, v52, v54
	v_max3_f32 v95, v95, v55, v72
	v_max3_f32 v96, v96, v74, v75
	v_max3_f32 v95, v95, v73, v56
	v_max3_f32 v96, v96, v58, v59
	v_max3_f32 v95, v95, v57, v76
	v_max3_f32 v96, v96, v78, v79
	v_max3_f32 v95, v95, v77, v60
	v_max3_f32 v96, v96, v62, v63
	v_max3_f32 v95, v95, v61, v80
	v_max3_f32 v96, v96, v82, v83
	v_max3_f32 v95, v95, v81, v64
	v_max3_f32 v96, v96, v66, v67
	v_max3_f32 v94, v95, v65, v96
	v_mov_b32_e32 v95, v94
	s_nop 1
	v_permlane32_swap_b32_e32 v94, v95
	v_max_f32_e32 v95, v95, v95
	v_max_f32_e32 v94, v94, v94
	v_max_f32_e32 v94, v94, v95
	v_cmp_lt_f32_e32 vcc, s14, v94
	s_cmp_lg_u64 vcc, 0
	s_cselect_b64 s[42:43], -1, 0
	s_cbranch_vccnz .LBB0_1284
; #define WAIT_BAR(N) asm volatile("s_waitcnt vmcnt(" #N ") lgkmcnt(0)\n\ts_barrier":::"memory")
;   #define RESC() do{ if(resc){ asm volatile("s_waitcnt lgkmcnt(0)":::"memory"); \
;       _Pragma("unroll") for(int d_=0;d_<2;++d_) _Pragma("unroll") for(int r=0;r<16;++r)o[d_][r]*=wsf[crow(r,hi)]; } }while(0)
;   #define ROT() do{sl_prev=sl_cur;sl_cur=sl_next;sl_next=(sl_next==(NSLOT-1)*SLOTB)?0:sl_next+SLOTB;}while(0)
; template<int THRL> __device__ __forceinline__ void attn_unit(int b,int h,int qb,const bf16*Q,const bf16*__restrict__ K,const bf16*__restrict__ V,bf16*O,const unsigned*MASK,char*shm){
;     ...
;   int t=1;
;   for(;t+5<NT;t+=2){
;     STEP(pB0,pB1,pA0,pA1,t,true,true,true,wB,wA);     WAIT_BAR(2); RESC(); ROT();
.LBB0_1277:
	s_waitcnt lgkmcnt(0)
	v_and_b32_e32 v146, v146, v114
	v_and_b32_e32 v147, v147, v115
	v_and_b32_e32 v148, v148, v116
	v_and_b32_e32 v149, v149, v117
	ds_read_b128 v[114:117], v226 offset:51200
	s_waitcnt lgkmcnt(14)
	v_mfma_f32_32x32x16_bf16 v[20:35], v[146:149], v[182:185], v[20:35]
	v_exp_f32_e32 v68, v68
	v_exp_f32_e32 v69, v69
	v_exp_f32_e32 v70, v70
	v_exp_f32_e32 v71, v71
	s_waitcnt lgkmcnt(12)
	v_mfma_f32_32x32x16_bf16 v[4:19], v[146:149], v[178:181], v[4:19]
	v_mfma_f32_32x32x16_bf16 v[228:243], v[146:149], v[204:207], v[228:243]
	v_exp_f32_e32 v72, v72
	v_exp_f32_e32 v73, v73
	v_exp_f32_e32 v74, v74
	v_exp_f32_e32 v75, v75
	s_waitcnt lgkmcnt(0)
	v_and_b32_e32 v142, v142, v114
	v_and_b32_e32 v143, v143, v115
	v_and_b32_e32 v144, v144, v116
	v_and_b32_e32 v145, v145, v117
	ds_read_b128 v[114:117], v248 offset:51200
	v_add_u32_e32 v94, s60, v221
	ds_read_b128 v[178:181], v94
	ds_read_b128 v[170:173], v94 offset:512
	s_waitcnt lgkmcnt(12)
	v_mfma_f32_32x32x16_bf16 v[20:35], v[142:145], v[150:153], v[20:35]
	v_exp_f32_e32 v76, v76
	v_exp_f32_e32 v77, v77
	v_exp_f32_e32 v78, v78
	v_exp_f32_e32 v79, v79
	ds_read_b128 v[174:177], v94 offset:2048
	ds_read_b128 v[162:165], v94 offset:2560
	s_waitcnt lgkmcnt(12)
	v_mfma_f32_32x32x16_bf16 v[4:19], v[142:145], v[110:113], v[4:19]
	v_mfma_f32_32x32x16_bf16 v[228:243], v[142:145], v[204:207], v[228:243]
	v_exp_f32_e32 v80, v80
	v_exp_f32_e32 v81, v81
	v_exp_f32_e32 v82, v82
	v_exp_f32_e32 v83, v83
	s_waitcnt lgkmcnt(4)
	v_and_b32_e32 v130, v130, v114
	v_and_b32_e32 v131, v131, v115
	v_and_b32_e32 v132, v132, v116
	v_and_b32_e32 v133, v133, v117
	ds_read_b128 v[114:117], v249 offset:51200
	ds_read_b128 v[166:169], v94 offset:4096
	ds_read_b128 v[154:157], v94 offset:4608
	s_waitcnt lgkmcnt(12)
	v_mfma_f32_32x32x16_bf16 v[20:35], v[130:133], v[106:109], v[20:35]
	v_exp_f32_e32 v52, v52
	v_exp_f32_e32 v53, v53
	v_exp_f32_e32 v54, v54
	v_exp_f32_e32 v55, v55
	ds_read_b128 v[158:161], v94 offset:6144
	ds_read_b128 v[150:153], v94 offset:6656
	s_waitcnt lgkmcnt(12)
	v_mfma_f32_32x32x16_bf16 v[4:19], v[130:133], v[102:105], v[4:19]
	v_mfma_f32_32x32x16_bf16 v[228:243], v[130:133], v[204:207], v[228:243]
	v_exp_f32_e32 v56, v56
	v_exp_f32_e32 v57, v57
	v_exp_f32_e32 v58, v58
	v_exp_f32_e32 v59, v59
	s_waitcnt lgkmcnt(4)
	v_and_b32_e32 v118, v118, v114
	v_and_b32_e32 v119, v119, v115
	v_and_b32_e32 v120, v120, v116
	v_and_b32_e32 v121, v121, v117
	s_nop 0
	s_waitcnt lgkmcnt(10)
	v_mfma_f32_32x32x16_bf16 v[20:35], v[118:121], v[90:93], v[20:35]
	v_exp_f32_e32 v60, v60
	v_exp_f32_e32 v61, v61
	v_exp_f32_e32 v62, v62
	v_exp_f32_e32 v63, v63
	s_waitcnt lgkmcnt(8)
	v_mfma_f32_32x32x16_bf16 v[4:19], v[118:121], v[86:89], v[4:19]
	v_mfma_f32_32x32x16_bf16 v[228:243], v[118:121], v[204:207], v[228:243]
	v_exp_f32_e32 v64, v64
	v_exp_f32_e32 v65, v65
	v_exp_f32_e32 v66, v66
	v_exp_f32_e32 v67, v67
	s_waitcnt vmcnt(3)
	v_lshlrev_b32_sdwa v225, s32, v2 dst_sel:DWORD dst_unused:UNUSED_PAD src0_sel:DWORD src1_sel:BYTE_0
	v_lshlrev_b32_sdwa v226, s32, v2 dst_sel:DWORD dst_unused:UNUSED_PAD src0_sel:DWORD src1_sel:BYTE_1
	v_lshlrev_b32_sdwa v248, s32, v2 dst_sel:DWORD dst_unused:UNUSED_PAD src0_sel:DWORD src1_sel:BYTE_2
	v_lshlrev_b32_sdwa v249, s32, v2 dst_sel:DWORD dst_unused:UNUSED_PAD src0_sel:DWORD src1_sel:BYTE_3
	s_waitcnt vmcnt(3) lgkmcnt(0)
	s_barrier
	s_andn2_b64 vcc, exec, s[42:43]
	s_cbranch_vccnz .LBB0_1279
	s_waitcnt lgkmcnt(0)
	ds_read_b128 v[86:89], v85 offset:49248
	ds_read_b128 v[90:93], v85 offset:49216
	ds_read_b128 v[94:97], v85 offset:49184
	ds_read_b128 v[98:101], v85 offset:49152
	s_waitcnt lgkmcnt(3)
	v_pk_mul_f32 v[32:33], v[32:33], v[86:87]
	s_waitcnt lgkmcnt(2)
	v_pk_mul_f32 v[28:29], v[28:29], v[90:91]
	s_waitcnt lgkmcnt(1)
	v_pk_mul_f32 v[24:25], v[24:25], v[94:95]
	v_pk_mul_f32 v[34:35], v[34:35], v[88:89]
	v_pk_mul_f32 v[30:31], v[30:31], v[92:93]
	v_pk_mul_f32 v[26:27], v[26:27], v[96:97]
	s_waitcnt lgkmcnt(0)
	v_pk_mul_f32 v[22:23], v[22:23], v[100:101]
	v_pk_mul_f32 v[20:21], v[20:21], v[98:99]
	v_pk_mul_f32 v[16:17], v[16:17], v[86:87]
	v_pk_mul_f32 v[12:13], v[12:13], v[90:91]
	v_pk_mul_f32 v[8:9], v[8:9], v[94:95]
	v_pk_mul_f32 v[18:19], v[18:19], v[88:89]
	v_pk_mul_f32 v[14:15], v[14:15], v[92:93]
	v_pk_mul_f32 v[10:11], v[10:11], v[96:97]
	v_pk_mul_f32 v[6:7], v[6:7], v[100:101]
	v_pk_mul_f32 v[4:5], v[4:5], v[98:99]
	v_pk_mul_f32 v[240:241], v[240:241], v[86:87]
	v_pk_mul_f32 v[236:237], v[236:237], v[90:91]
	v_pk_mul_f32 v[232:233], v[232:233], v[94:95]
	v_pk_mul_f32 v[242:243], v[242:243], v[88:89]
	v_pk_mul_f32 v[238:239], v[238:239], v[92:93]
	v_pk_mul_f32 v[234:235], v[234:235], v[96:97]
	v_pk_mul_f32 v[230:231], v[230:231], v[100:101]
	v_pk_mul_f32 v[228:229], v[228:229], v[98:99]

;   #define RESC() do{ if(resc){ asm volatile("s_waitcnt lgkmcnt(0)":::"memory"); \
;       _Pragma("unroll") for(int d_=0;d_<2;++d_) _Pragma("unroll") for(int r=0;r<16;++r)o[d_][r]*=wsf[crow(r,hi)]; } }while(0)
;   #define ROT() do{sl_prev=sl_cur;sl_cur=sl_next;sl_next=(sl_next==(NSLOT-1)*SLOTB)?0:sl_next+SLOTB;}while(0)
;   #define ENDW(tt) do{ if((tt)+3<NT){WAIT_BAR(2);} else if((tt)+2<NT){WAIT_BAR(1);} else {WAIT_BAR(0);} }while(0)
; template<int THRL> __device__ __forceinline__ void attn_unit(int b,int h,int qb,const bf16*Q,const bf16*__restrict__ K,const bf16*__restrict__ V,bf16*O,const unsigned*MASK,char*shm){
;     ...
;   for(;t+1<NT;t+=2){
;     STEP(pB0,pB1,pA0,pA1,t,(t+3<NT),(t+1<NT),(t+1<NT),wB,wA);       ENDW(t);   RESC(); ROT();
;     STEP(pA0,pA1,pB0,pB1,t+1,(t+4<NT),(t+2<NT),(t+2<NT),wA,wB);     ENDW(t+1); RESC(); ROT();
.LBB0_1288:
	s_waitcnt vmcnt(0)
	s_add_i32 s4, s92, 1
	s_cmp_ge_i32 s4, s61
	s_cbranch_scc1 .LBB0_1336
	v_lshlrev_b32_e32 v85, 4, v214
	s_lshl_b64 s[4:5], s[92:93], 8
	s_add_i32 s63, s61, -2
	v_cmp_gt_u32_e64 s[40:41], 32, v1
	v_lshl_add_u32 v2, v213, 2, s57
	s_lshl_b64 s[46:47], s[92:93], 16
	v_lshl_add_u64 v[210:211], v[186:187], 0, s[4:5]
	s_add_i32 s64, s92, 4
	v_add_u32_e32 v222, s57, v85
